# A/B: P1 loop bookkeeping left at hipcc positions (outside the MFMA run), everything else as the current best
# baseline (speedup 1.0000x reference)
.LBB2_34:
	ds_read_b128 v[144:147], v203
	ds_read_b128 v[148:151], v203 offset:2048
	ds_read_b128 v[156:159], v204
	ds_read_b128 v[152:155], v204 offset:2048
	s_cmp_lg_u32 s74, 12
	s_cselect_b64 s[0:1], -1, 0
	s_and_b64 s[4:5], s[0:1], exec
	s_cselect_b32 s75, s73, s68
	s_cselect_b32 s16, s72, s69
	s_mov_b32 m0, s53
	s_and_b32 s5, s71, 0xffff
	s_mov_b32 s4, s70
	ds_read_b128 v[184:187], v205
	ds_read_b128 v[172:175], v205 offset:2048
	ds_read_b128 v[188:191], v206
	ds_read_b128 v[176:179], v206 offset:2048
	ds_read_b128 v[168:171], v205 offset:4096
	ds_read_b128 v[160:163], v205 offset:6144
	ds_read_b128 v[180:183], v206 offset:4096
	ds_read_b128 v[164:167], v206 offset:6144
	buffer_load_dwordx4 v193, s[4:7], 0 offen lds
	s_mov_b32 m0, s54
	s_or_b64 s[36:37], s[28:29], s[0:1]
	buffer_load_dwordx4 v197, s[4:7], 0 offen lds
	s_waitcnt lgkmcnt(8)
	s_barrier
	s_waitcnt lgkmcnt(0)
	s_xor_b64 s[34:35], s[36:37], -1
	s_setprio 1
	v_mfma_i32_16x16x64_i8 v[124:127], v[144:147], v[184:187], v[124:127]
	v_mfma_i32_16x16x64_i8 v[120:123], v[148:151], v[184:187], v[120:123]
	v_mfma_i32_16x16x64_i8 v[108:111], v[144:147], v[172:175], v[108:111]
	v_mfma_i32_16x16x64_i8 v[104:107], v[148:151], v[172:175], v[104:107]
	v_mfma_i32_16x16x64_i8 v[96:99], v[144:147], v[168:171], v[96:99]
	v_mfma_i32_16x16x64_i8 v[88:91], v[148:151], v[168:171], v[88:91]
	v_mfma_i32_16x16x64_i8 v[80:83], v[144:147], v[160:163], v[80:83]
	v_mfma_i32_16x16x64_i8 v[72:75], v[148:151], v[160:163], v[72:75]
	v_mfma_i32_16x16x64_i8 v[124:127], v[156:159], v[188:191], v[124:127]
	v_mfma_i32_16x16x64_i8 v[120:123], v[152:155], v[188:191], v[120:123]
	v_mfma_i32_16x16x64_i8 v[108:111], v[156:159], v[176:179], v[108:111]
	v_mfma_i32_16x16x64_i8 v[104:107], v[152:155], v[176:179], v[104:107]
	v_mfma_i32_16x16x64_i8 v[96:99], v[156:159], v[180:183], v[96:99]
	v_mfma_i32_16x16x64_i8 v[88:91], v[152:155], v[180:183], v[88:91]
	v_mfma_i32_16x16x64_i8 v[80:83], v[156:159], v[164:167], v[80:83]
	v_mfma_i32_16x16x64_i8 v[72:75], v[152:155], v[164:167], v[72:75]
	s_setprio 0
	s_barrier
	ds_read_b128 v[128:131], v207
	ds_read_b128 v[132:135], v207 offset:2048
	ds_read_b128 v[140:143], v208
	ds_read_b128 v[136:139], v208 offset:2048
	s_and_b64 vcc, exec, s[34:35]
	s_cbranch_vccnz .LBB2_36
	s_and_b32 s17, s75, 0xffff
	s_mov_b32 s18, s6
	s_mov_b32 s19, s7
	s_mov_b32 m0, s39
	s_nop 0
	buffer_load_dwordx4 v196, s[16:19], 0 offen lds
	s_mov_b32 m0, s40
	s_nop 0
	buffer_load_dwordx4 v198, s[16:19], 0 offen lds
.LBB2_36:
	s_add_u32 s4, s70, 0xfffc0080
	s_addc_u32 s5, s71, -1
	s_barrier
	s_waitcnt lgkmcnt(0)
	s_and_b64 s[0:1], s[0:1], exec
	s_cselect_b32 s17, s5, s66
	s_cselect_b32 s4, s4, s67
	s_setprio 1
	v_mfma_i32_16x16x64_i8 v[116:119], v[128:131], v[184:187], v[116:119]
	v_mfma_i32_16x16x64_i8 v[112:115], v[132:135], v[184:187], v[112:115]
	v_mfma_i32_16x16x64_i8 v[100:103], v[128:131], v[172:175], v[100:103]
	v_mfma_i32_16x16x64_i8 v[92:95], v[132:135], v[172:175], v[92:95]
	v_mfma_i32_16x16x64_i8 v[84:87], v[128:131], v[168:171], v[84:87]
	v_mfma_i32_16x16x64_i8 v[76:79], v[132:135], v[168:171], v[76:79]
	v_mfma_i32_16x16x64_i8 v[68:71], v[128:131], v[160:163], v[68:71]
	v_mfma_i32_16x16x64_i8 v[64:67], v[132:135], v[160:163], v[64:67]
	v_mfma_i32_16x16x64_i8 v[116:119], v[140:143], v[188:191], v[116:119]
	v_mfma_i32_16x16x64_i8 v[112:115], v[136:139], v[188:191], v[112:115]
	v_mfma_i32_16x16x64_i8 v[100:103], v[140:143], v[176:179], v[100:103]
	v_mfma_i32_16x16x64_i8 v[92:95], v[136:139], v[176:179], v[92:95]
	v_mfma_i32_16x16x64_i8 v[84:87], v[140:143], v[180:183], v[84:87]
	v_mfma_i32_16x16x64_i8 v[76:79], v[136:139], v[180:183], v[76:79]
	v_mfma_i32_16x16x64_i8 v[68:71], v[140:143], v[164:167], v[68:71]
	v_mfma_i32_16x16x64_i8 v[64:67], v[136:139], v[164:167], v[64:67]
	s_setprio 0
	s_barrier
	ds_read_b128 v[184:187], v205 offset:16384
	ds_read_b128 v[172:175], v205 offset:18432
	ds_read_b128 v[188:191], v206 offset:16384
	ds_read_b128 v[176:179], v206 offset:18432
	ds_read_b128 v[168:171], v205 offset:20480
	ds_read_b128 v[160:163], v205 offset:22528
	ds_read_b128 v[180:183], v206 offset:20480
	ds_read_b128 v[164:167], v206 offset:22528
	v_cndmask_b32_e64 v194, 0, 1, s[36:37]
	v_cmp_ne_u32_e64 s[0:1], 1, v194
	s_andn2_b64 vcc, exec, s[36:37]
	s_cbranch_vccnz .LBB2_38
	s_and_b32 s5, s17, 0xffff
	s_mov_b32 m0, s38
	s_nop 0
	buffer_load_dwordx4 v193, s[4:7], 0 offen lds
	s_mov_b32 m0, s41
	s_nop 0
	buffer_load_dwordx4 v197, s[4:7], 0 offen lds

amdhsa.kernels:
  - .agpr_count:     0
    .args:
      - .actual_access:  read_only
        .address_space:  global
        .offset:         0
        .size:           8
        .value_kind:     global_buffer
      - .actual_access:  read_only
        .address_space:  global
        .offset:         8
        .size:           8
        .value_kind:     global_buffer
      - .actual_access:  read_only
        .address_space:  global
        .offset:         16
        .size:           8
        .value_kind:     global_buffer
      - .actual_access:  read_only
        .address_space:  global
        .offset:         24
        .size:           8
        .value_kind:     global_buffer
      - .actual_access:  read_only
        .address_space:  global
        .offset:         32
        .size:           8
        .value_kind:     global_buffer
      - .actual_access:  read_only
        .address_space:  global
        .offset:         40
        .size:           8
        .value_kind:     global_buffer
      - .actual_access:  read_only
        .address_space:  global
        .offset:         48
        .size:           8
        .value_kind:     global_buffer
      - .actual_access:  read_only
        .address_space:  global
        .offset:         56
        .size:           8
        .value_kind:     global_buffer
      - .actual_access:  write_only
        .address_space:  global
        .offset:         64
        .size:           8
        .value_kind:     global_buffer
      - .offset:         72
        .size:           4
        .value_kind:     by_value
    .group_segment_fixed_size: 32768
    .kernarg_segment_align: 8
    .kernarg_segment_size: 76
    .language:       OpenCL C
    .language_version:
      - 2
      - 0
    .max_flat_workgroup_size: 256
    .name:           _ZN2rb6k_prepEPKfS1_S1_S1_S1_S1_S1_S1_Phi
    .private_segment_fixed_size: 0
    .sgpr_count:     22
    .sgpr_spill_count: 0
    .symbol:         _ZN2rb6k_prepEPKfS1_S1_S1_S1_S1_S1_S1_Phi.kd
    .uniform_work_group_size: 1
    .uses_dynamic_stack: false
    .vgpr_count:     100
    .vgpr_spill_count: 0
    .wavefront_size: 64
  - .agpr_count:     0
    .args:
      - .address_space:  global
        .offset:         0
        .size:           8
        .value_kind:     global_buffer
      - .actual_access:  read_only
        .address_space:  global
        .offset:         8
        .size:           8
        .value_kind:     global_buffer
    .group_segment_fixed_size: 0
    .kernarg_segment_align: 8
    .kernarg_segment_size: 16
    .language:       OpenCL C
    .language_version:
      - 2
      - 0
    .max_flat_workgroup_size: 256
    .name:           _ZN2rb5k_midEPhPKf
    .private_segment_fixed_size: 0
    .sgpr_count:     20
    .sgpr_spill_count: 0
    .symbol:         _ZN2rb5k_midEPhPKf.kd
    .uniform_work_group_size: 1
    .uses_dynamic_stack: false
    .vgpr_count:     86
    .vgpr_spill_count: 0
    .wavefront_size: 64
  - .agpr_count:     0
    .args:
      - .offset:         0
        .size:           24
        .value_kind:     by_value
      - .offset:         24
        .size:           64
        .value_kind:     by_value
    .group_segment_fixed_size: 0
    .kernarg_segment_align: 8
    .kernarg_segment_size: 88
    .language:       OpenCL C
    .language_version:
      - 2
      - 0
    .max_flat_workgroup_size: 512
    .name:           _ZN2rb6k_gemmILi2ENS_7SchedP1ENS_5EpiP1EEEvT0_T1_
    .private_segment_fixed_size: 0
    .sgpr_count:     86
    .sgpr_spill_count: 0
    .symbol:         _ZN2rb6k_gemmILi2ENS_7SchedP1ENS_5EpiP1EEEvT0_T1_.kd
    .uniform_work_group_size: 1
    .uses_dynamic_stack: false
    .vgpr_count:     209
    .vgpr_spill_count: 0
    .wavefront_size: 64
  - .agpr_count:     0
    .args:
      - .offset:         0
        .size:           24
        .value_kind:     by_value
      - .offset:         24
        .size:           16
        .value_kind:     by_value
    .group_segment_fixed_size: 0
    .kernarg_segment_align: 8
    .kernarg_segment_size: 40
    .language:       OpenCL C
    .language_version:
      - 2
      - 0
    .max_flat_workgroup_size: 512
    .name:           _ZN2rb6k_gemmILi1ENS_7SchedP2ENS_7EpiSlabEEEvT0_T1_
    .private_segment_fixed_size: 0
    .sgpr_count:     73
    .sgpr_spill_count: 0
    .symbol:         _ZN2rb6k_gemmILi1ENS_7SchedP2ENS_7EpiSlabEEEvT0_T1_.kd
    .uniform_work_group_size: 1
    .uses_dynamic_stack: false
    .vgpr_count:     210
    .vgpr_spill_count: 0
    .wavefront_size: 64
  - .agpr_count:     0
    .args:
      - .offset:         0
        .size:           32
        .value_kind:     by_value
      - .offset:         32
        .size:           16
        .value_kind:     by_value
    .group_segment_fixed_size: 0
    .kernarg_segment_align: 8
    .kernarg_segment_size: 48
    .language:       OpenCL C
    .language_version:
      - 2
      - 0
    .max_flat_workgroup_size: 512
    .name:           _ZN2rb6k_gemmILi1ENS_6SchedGILb1EEENS_5EpiP3EEEvT0_T1_
    .private_segment_fixed_size: 0
    .sgpr_count:     62
    .sgpr_spill_count: 0
    .symbol:         _ZN2rb6k_gemmILi1ENS_6SchedGILb1EEENS_5EpiP3EEEvT0_T1_.kd
    .uniform_work_group_size: 1
    .uses_dynamic_stack: false
    .vgpr_count:     207
    .vgpr_spill_count: 0
    .wavefront_size: 64
  - .agpr_count:     0
    .args:
      - .offset:         0
        .size:           32
        .value_kind:     by_value
      - .offset:         32
        .size:           48
        .value_kind:     by_value
    .group_segment_fixed_size: 0
    .kernarg_segment_align: 8
    .kernarg_segment_size: 80
    .language:       OpenCL C
    .language_version:
      - 2
      - 0
    .max_flat_workgroup_size: 512
    .name:           _ZN2rb6k_gemmILi1ENS_6SchedGILb1EEENS_6EpiOutEEEvT0_T1_
    .private_segment_fixed_size: 0
    .sgpr_count:     62
    .sgpr_spill_count: 0
    .symbol:         _ZN2rb6k_gemmILi1ENS_6SchedGILb1EEENS_6EpiOutEEEvT0_T1_.kd
    .uniform_work_group_size: 1
    .uses_dynamic_stack: false
    .vgpr_count:     205
    .vgpr_spill_count: 0
    .wavefront_size: 64
  - .agpr_count:     0
    .args:
      - .offset:         0
        .size:           24
        .value_kind:     by_value
      - .offset:         24
        .size:           1
        .value_kind:     by_value
    .group_segment_fixed_size: 0
    .kernarg_segment_align: 8
    .kernarg_segment_size: 28
    .language:       OpenCL C
    .language_version:
      - 2
      - 0
    .max_flat_workgroup_size: 512
    .name:           _ZN2rb6k_gemmILi2ENS_7SchedP1ENS_7EpiNullEEEvT0_T1_
    .private_segment_fixed_size: 0
    .sgpr_count:     66
    .sgpr_spill_count: 0
    .symbol:         _ZN2rb6k_gemmILi2ENS_7SchedP1ENS_7EpiNullEEEvT0_T1_.kd
    .uniform_work_group_size: 1
    .uses_dynamic_stack: false
    .vgpr_count:     205
    .vgpr_spill_count: 0
    .wavefront_size: 64
